# priority: toggles removed plus one static raise for waves 4-7 during GEMM phases
# baseline (speedup 1.0000x reference)
.LBB0_297:
	s_or_b64 exec, exec, s[0:1]
	v_readlane_b32 s0, v242, 51
	s_add_u32 s2, s0, 0x3b600000
	v_readlane_b32 s0, v242, 52
	s_addc_u32 s3, s0, 0
	v_writelane_b32 v242, s2, 53
	s_mov_b32 s0, s86
	s_waitcnt lgkmcnt(0)
	v_writelane_b32 v242, s3, 54
	s_mov_b32 s2, s79
	s_waitcnt vmcnt(0)
	s_barrier
	s_cselect_b32 s101, 1, 0
	v_readlane_b32 s100, v242, 48
	s_nop 3
	s_cmp_lt_u32 s100, 4
	s_cbranch_scc1 .Lgp_0
	s_setprio 1
.Lgp_0:
	s_cmp_lg_u32 s101, 0
	v_mbcnt_lo_u32_b32 v0, -1, 0
	v_mbcnt_hi_u32_b32 v0, -1, v0
	s_mov_b32 s4, s28
	s_waitcnt vmcnt(12)
	v_lshl_add_u32 v14, s0, 6, v0
	v_readlane_b32 s0, v243, 41
	s_mov_b32 s5, s79
	v_readlane_b32 s1, v243, 42
	s_andn2_b64 vcc, exec, s[0:1]
	v_readfirstlane_b32 s3, v14
	v_writelane_b32 v242, s4, 55
	s_nop 1
	v_writelane_b32 v242, s5, 56
	s_cbranch_vccnz .LBB0_333
	v_lshlrev_b32_e32 v0, 4, v14
	v_add_u32_e32 v1, 0x2000, v0
	v_ashrrev_i32_e32 v2, 31, v1
	v_lshrrev_b32_e32 v2, 22, v2
	v_add_u32_e32 v2, v1, v2
	v_ashrrev_i32_e32 v8, 10, v2
	v_mul_i32_i24_e32 v2, 0x400, v8
	v_sub_u32_e32 v1, v1, v2
	v_lshrrev_b32_e32 v2, 4, v1
	v_bitop3_b32 v1, v2, v1, 32 bitop3:0x6c
	v_ashrrev_i32_e32 v2, 31, v1
	s_mul_hi_u32 s0, s4, 0x900000
	s_mul_i32 s1, s4, 0x900000
	v_readlane_b32 s4, v242, 51
	v_lshrrev_b32_e32 v2, 26, v2
	s_add_u32 s1, s4, s1
	v_readlane_b32 s4, v242, 52
	v_add_u32_e32 v2, v1, v2
	v_lshlrev_b32_e32 v3, 3, v8
	s_addc_u32 s0, s4, s0
	v_ashrrev_i32_e32 v9, 6, v2
	v_and_b32_e32 v3, -16, v3
	s_add_u32 s30, s1, 0x800000
	v_add_u32_e32 v3, v9, v3
	s_addc_u32 s31, s0, 0
	v_and_b32_e32 v4, 3, v9
	s_mov_b32 s0, 0x1fffe0
	v_lshrrev_b32_e32 v5, 2, v3
	v_lshlrev_b32_e32 v6, 1, v3
	v_and_b32_e32 v2, 0xc0, v2
	v_and_or_b32 v4, v3, s0, v4
	v_and_b32_e32 v5, 4, v5
	v_and_b32_e32 v6, 24, v6
	v_sub_u32_e32 v1, v1, v2
	v_or3_b32 v4, v4, v5, v6
	v_lshlrev_b32_e32 v5, 5, v8
	v_ashrrev_i16_sdwa v1, v201, sext(v1) dst_sel:DWORD dst_unused:UNUSED_PAD src0_sel:DWORD src1_sel:BYTE_0
	v_and_b32_e32 v5, 32, v5
	v_bfe_i32 v10, v1, 0, 16
	v_add_lshl_u32 v1, v5, v10, 1
	v_lshl_add_u32 v146, v4, 11, v1
	v_lshl_add_u32 v148, v3, 11, v1
	v_bfe_i32 v1, v14, 27, 1
	v_lshrrev_b32_e32 v1, 22, v1
	v_add_u32_e32 v1, v0, v1
	v_and_b32_e32 v1, 0xfffffc00, v1
	v_sub_u32_e32 v0, v0, v1
	v_lshrrev_b32_e32 v1, 4, v0
	v_bitop3_b32 v1, v1, v0, 32 bitop3:0x6c
	v_ashrrev_i32_e32 v0, 31, v0
	v_lshrrev_b32_e32 v0, 26, v0
	v_add_u32_e32 v0, v1, v0
	v_ashrrev_i32_e32 v11, 6, v0
	v_ashrrev_i32_e32 v0, 31, v14
	v_lshrrev_b32_e32 v0, 26, v0
	v_add_u32_e32 v0, v14, v0
	v_ashrrev_i32_e32 v12, 6, v0
	v_lshlrev_b32_e32 v0, 3, v12
	v_and_b32_e32 v0, -16, v0
	v_add_u32_e32 v0, v11, v0
	s_ashr_i32 s6, s3, 6
	v_and_b32_e32 v2, 3, v11
	v_lshrrev_b32_e32 v3, 2, v0
	v_lshlrev_b32_e32 v4, 1, v0
	s_ashr_i32 s5, s3, 8
	s_lshl_b32 s4, s6, 10
	v_and_or_b32 v2, v0, s0, v2
	v_and_b32_e32 v3, 4, v3
	v_and_b32_e32 v4, 24, v4
	v_readlane_b32 s0, v242, 26
	v_or3_b32 v2, v2, v3, v4
	v_mul_i32_i24_e32 v4, 64, v11
	v_readlane_b32 s1, v242, 27
	s_add_u32 s26, s30, s0
	v_sub_u32_e32 v1, v1, v4
	s_addc_u32 s27, s31, s1
	s_add_i32 s34, s2, 0x10000
	v_lshlrev_b32_e32 v3, 5, v12
	v_ashrrev_i16_sdwa v1, v201, sext(v1) dst_sel:DWORD dst_unused:UNUSED_PAD src0_sel:DWORD src1_sel:BYTE_0
	s_add_i32 s35, s34, s4
	v_and_b32_e32 v3, 32, v3
	v_bfe_i32 v13, v1, 0, 16
	s_add_i32 s36, s35, 0x2000
	v_add_lshl_u32 v1, v3, v13, 1
	s_add_u32 s0, s26, 0x40000
	v_lshl_add_u32 v150, v2, 11, v1
	s_mov_b32 m0, s35
	s_addc_u32 s1, s27, 0
	s_add_i32 s37, s2, 0x14000
	global_load_lds_dwordx4 v150, s[26:27]
	s_mov_b32 m0, s36
	s_add_i32 s38, s37, s4
	global_load_lds_dwordx4 v146, s[26:27]
	s_mov_b32 m0, s38
	s_add_i32 s39, s38, 0x2000
	global_load_lds_dwordx4 v150, s[0:1]
	s_mov_b32 m0, s39
	v_readlane_b32 s8, v242, 53
	global_load_lds_dwordx4 v146, s[0:1]
	v_readlane_b32 s0, v242, 36
	v_readlane_b32 s1, v242, 37
	v_readlane_b32 s9, v242, 54
	s_add_u32 s24, s8, s0
	s_addc_u32 s25, s9, s1
	s_add_i32 s40, s2, s4
	s_add_i32 s41, s40, 0x2000
	v_lshl_add_u32 v152, v0, 11, v1
	s_mov_b32 m0, s40
	s_add_u32 s0, s24, 0x40000
	global_load_lds_dwordx4 v152, s[24:25]
	s_mov_b32 m0, s41
	s_addc_u32 s1, s25, 0
	s_add_i32 s42, s40, 0x4000
	global_load_lds_dwordx4 v148, s[24:25]
	s_mov_b32 m0, s42
	s_add_i32 s43, s40, 0x6000
	global_load_lds_dwordx4 v152, s[0:1]
	s_mov_b32 m0, s43
	v_mov_b32_e32 v151, v65
	global_load_lds_dwordx4 v148, s[0:1]
	v_mov_b32_e32 v147, v65
	v_mov_b32_e32 v153, v65
	v_mov_b32_e32 v149, v65
	s_cmp_eq_u32 s5, 1
	v_lshl_add_u64 v[6:7], s[26:27], 0, v[150:151]
	v_lshl_add_u64 v[4:5], s[26:27], 0, v[146:147]
	v_lshl_add_u64 v[0:1], s[24:25], 0, v[152:153]
	s_cselect_b64 s[0:1], -1, 0
	s_cmp_lg_u32 s5, 1
	v_lshl_add_u64 v[2:3], s[24:25], 0, v[148:149]
	s_cbranch_scc1 .LBB0_300
	s_barrier

.LBB0_358:
	s_mov_b32 s2, s84
	s_waitcnt vmcnt(0)
	s_waitcnt vmcnt(0)
	s_setprio 0
	s_barrier
	v_readlane_b32 s100, v242, 48
	s_nop 3
	s_cmp_lg_u32 s100, 1
	s_cbranch_scc1 .Lxb_skipinv_3
	buffer_inv sc1

.LBB0_805:
	s_or_b64 exec, exec, s[0:1]
	v_readlane_b32 s2, v242, 55
	s_cmp_eq_u32 s2, 0
	s_mov_b64 s[6:7], 0
	s_cselect_b64 s[0:1], -1, 0
	s_cmp_lg_u32 s2, 0
	s_mov_b64 s[8:9], 0
	s_waitcnt lgkmcnt(0)
	s_waitcnt vmcnt(0)
	s_barrier
	s_cselect_b32 s101, 1, 0
	v_readlane_b32 s100, v242, 48
	s_nop 3
	s_cmp_lt_u32 s100, 4
	s_cbranch_scc1 .Lgp_1
	s_setprio 1
.Lgp_1:
	s_cmp_lg_u32 s101, 0
	v_readlane_b32 s3, v242, 56
	s_cbranch_scc0 .LBB0_899
	s_andn2_b64 vcc, exec, s[0:1]
	s_cbranch_vccz .LBB0_900

.LBB0_920:
	s_mov_b32 s2, s84
	s_waitcnt vmcnt(0)
	s_setprio 0
	s_barrier
	v_readlane_b32 s100, v242, 48
	s_nop 3
	s_cmp_lg_u32 s100, 1
	s_cbranch_scc1 .Lxb_skipinv_7
	buffer_inv sc1

.LBB0_1378:
	s_or_b64 exec, exec, s[0:1]
	v_readlane_b32 s0, v241, 10
	v_readlane_b32 s1, v241, 11
	s_and_b64 s[0:1], s[0:1], exec
	s_cselect_b32 s33, 16, 17
	s_mov_b32 s4, s79
	s_mov_b32 s0, s86
	s_waitcnt lgkmcnt(0)
	s_waitcnt vmcnt(0)
	s_barrier
	s_cselect_b32 s101, 1, 0
	v_readlane_b32 s100, v242, 48
	s_nop 3
	s_cmp_lt_u32 s100, 4
	s_cbranch_scc1 .Lgp_2
	s_setprio 1
.Lgp_2:
	s_cmp_lg_u32 s101, 0
	v_mbcnt_lo_u32_b32 v0, -1, 0
	v_mbcnt_hi_u32_b32 v0, -1, v0
	s_lshl_b32 s34, s33, 4
	v_lshl_add_u32 v1, s0, 6, v0
	v_cvt_f32_u32_e32 v0, s34
	s_lshl_b32 s35, s33, 8
	s_cmp_lt_i32 s71, s35
	v_rcp_iflag_f32_e32 v0, v0
	s_cselect_b64 s[0:1], -1, 0
	s_cmp_ge_i32 s71, s35
	v_readfirstlane_b32 s5, v1
	s_cbranch_scc1 .LBB0_1383
	v_mul_f32_e32 v2, 0x4f7ffffe, v0
	v_cvt_u32_f32_e32 v2, v2
	s_sub_i32 s2, 0, s34
	v_readlane_b32 s7, v242, 31
	v_readfirstlane_b32 s3, v2
	s_mul_i32 s2, s2, s3
	s_mul_hi_u32 s2, s3, s2
	s_add_i32 s3, s3, s2
	s_mul_hi_u32 s2, s7, s3
	s_mul_i32 s3, s2, s34
	s_sub_i32 s3, s7, s3
	s_add_i32 s6, s2, 1
	s_sub_i32 s7, s3, s34
	s_cmp_ge_u32 s3, s34
	s_cselect_b32 s2, s6, s2
	s_cselect_b32 s3, s7, s3
	s_add_i32 s6, s2, 1
	s_cmp_ge_u32 s3, s34
	s_cselect_b32 s2, s6, s2
	v_readlane_b32 s3, v242, 30
	s_xor_b32 s2, s2, s3
	s_sub_i32 s6, s2, s3
	s_mul_i32 s2, s6, s34
	s_sub_i32 s7, s71, s2
	s_cmpk_gt_i32 s7, 0xff
	s_mul_i32 s8, s6, 17
	s_mov_b64 s[2:3], -1
	s_cbranch_scc0 .LBB0_1381
	s_lshr_b32 s2, s7, 4
	s_add_i32 s63, s2, s8
	s_lshl_b32 s2, s6, 4
	v_readlane_b32 s3, v242, 19
	s_or_b32 s18, s2, s3
	s_mov_b64 s[2:3], 0

.LBB0_1414:
	s_mov_b32 s10, s84
	s_waitcnt vmcnt(0)
	s_waitcnt vmcnt(0) lgkmcnt(0)
	s_setprio 0
	s_barrier
	v_readlane_b32 s100, v242, 48
	s_nop 3
	s_cmp_lg_u32 s100, 1
	s_cbranch_scc1 .Lxb_skipinv_10
	buffer_inv sc1

.LBB0_1466:
	s_or_b64 exec, exec, s[0:1]
	s_mov_b32 s12, s79
	s_mov_b32 s0, s86
	s_waitcnt lgkmcnt(0)
	s_waitcnt vmcnt(0)
	s_barrier
	s_cselect_b32 s101, 1, 0
	v_readlane_b32 s100, v242, 48
	s_nop 3
	s_cmp_lt_u32 s100, 4
	s_cbranch_scc1 .Lgp_3
	s_setprio 1
.Lgp_3:
	s_cmp_lg_u32 s101, 0
	v_mbcnt_lo_u32_b32 v0, -1, 0
	v_mbcnt_hi_u32_b32 v0, -1, v0
	s_lshl_b32 s38, s33, 6
	v_lshl_add_u32 v0, s0, 6, v0
	s_cmp_ge_i32 s71, s38
	v_readfirstlane_b32 s10, v0
	s_cbranch_scc1 .LBB0_1490
	v_bfe_i32 v3, v0, 27, 1
	v_lshlrev_b32_e32 v1, 4, v0
	v_lshrrev_b32_e32 v3, 22, v3
	v_add_u32_e32 v3, v1, v3
	v_and_b32_e32 v3, 0xfffffc00, v3
	v_sub_u32_e32 v3, v1, v3
	v_ashrrev_i32_e32 v2, 31, v0
	v_lshrrev_b32_e32 v4, 4, v3
	v_lshrrev_b32_e32 v2, 26, v2
	v_bitop3_b32 v4, v4, v3, 32 bitop3:0x6c
	v_ashrrev_i32_e32 v3, 31, v3
	v_readlane_b32 s0, v242, 55
	v_add_u32_e32 v2, v0, v2
	v_lshrrev_b32_e32 v3, 26, v3
	v_readlane_b32 s1, v242, 56
	v_ashrrev_i32_e32 v2, 6, v2
	v_add_u32_e32 v3, v4, v3
	s_lshl_b64 s[0:1], s[0:1], 25
	v_readlane_b32 s2, v242, 51
	v_lshlrev_b32_e32 v5, 3, v2
	v_ashrrev_i32_e32 v3, 6, v3
	s_add_u32 s0, s2, s0
	v_readlane_b32 s2, v242, 52
	v_and_b32_e32 v5, -16, v5
	v_mul_i32_i24_e32 v6, 64, v3
	s_addc_u32 s1, s2, s1
	v_add_u32_e32 v5, v3, v5
	v_sub_u32_e32 v4, v4, v6
	s_add_u32 s39, s0, 0x23400000
	v_lshlrev_b32_e32 v2, 5, v2
	v_ashrrev_i16_sdwa v4, v201, sext(v4) dst_sel:DWORD dst_unused:UNUSED_PAD src0_sel:DWORD src1_sel:BYTE_0
	v_lshlrev_b32_e32 v6, 1, v5
	v_lshrrev_b32_e32 v7, 2, v5
	v_and_b32_e32 v3, 3, v3
	s_mov_b32 s0, 0x1fffe0
	v_and_b32_e32 v2, 32, v2
	v_bfe_i32 v4, v4, 0, 16
	v_and_b32_e32 v6, 24, v6
	v_and_b32_e32 v7, 4, v7
	v_and_or_b32 v3, v5, s0, v3
	v_or3_b32 v3, v3, v7, v6
	v_add_lshl_u32 v2, v2, v4, 1
	v_add_u32_e32 v1, 0x2000, v1
	v_lshl_add_u32 v211, v3, 11, v2
	v_lshl_add_u32 v212, v5, 11, v2
	v_ashrrev_i32_e32 v2, 31, v1
	v_lshrrev_b32_e32 v2, 22, v2
	v_add_u32_e32 v2, v1, v2
	v_ashrrev_i32_e32 v2, 10, v2
	v_mul_i32_i24_e32 v3, 0x400, v2
	v_sub_u32_e32 v1, v1, v3
	v_lshrrev_b32_e32 v3, 4, v1
	v_bitop3_b32 v1, v3, v1, 32 bitop3:0x6c
	v_ashrrev_i32_e32 v4, 31, v1
	v_lshrrev_b32_e32 v4, 26, v4
	v_lshlrev_b32_e32 v3, 3, v2
	v_add_u32_e32 v4, v1, v4
	v_and_b32_e32 v3, -16, v3
	v_ashrrev_i32_e32 v5, 6, v4
	v_add_u32_e32 v3, v5, v3
	v_and_b32_e32 v4, 0xc0, v4
	v_sub_u32_e32 v1, v1, v4
	v_lshlrev_b32_e32 v4, 1, v3
	v_lshrrev_b32_e32 v6, 2, v3
	v_and_b32_e32 v5, 3, v5
	s_addc_u32 s40, s1, 0
	v_and_b32_e32 v4, 24, v4
	v_and_b32_e32 v6, 4, v6
	v_and_or_b32 v5, v3, s0, v5
	s_lshl_b32 s33, s33, 2
	v_or3_b32 v4, v5, v6, v4
	v_cvt_f32_ubyte0_e32 v5, s33
	v_rcp_iflag_f32_e32 v5, v5
	v_lshlrev_b32_e32 v2, 5, v2
	v_ashrrev_i16_sdwa v1, v201, sext(v1) dst_sel:DWORD dst_unused:UNUSED_PAD src0_sel:DWORD src1_sel:BYTE_0
	v_and_b32_e32 v2, 32, v2
	v_bfe_i32 v1, v1, 0, 16
	v_add_lshl_u32 v1, v2, v1, 1
	v_lshl_add_u32 v213, v4, 11, v1
	v_lshl_add_u32 v214, v3, 11, v1
	v_mul_f32_e32 v1, 0x4f7ffffe, v5
	v_cvt_u32_f32_e32 v1, v1
	s_sub_i32 s0, 0, s33
	v_readlane_b32 s2, v242, 31
	s_ashr_i32 s14, s10, 6
	v_readfirstlane_b32 s41, v1
	s_mul_i32 s0, s0, s41
	s_mul_hi_u32 s0, s41, s0
	s_add_i32 s41, s41, s0
	s_mul_hi_u32 s0, s2, s41
	s_mul_i32 s1, s0, s33
	s_sub_i32 s1, s2, s1
	s_ashr_i32 s13, s10, 8
	s_lshl_b32 s11, s14, 10
	s_add_i32 s2, s0, 1
	s_sub_i32 s3, s1, s33
	s_cmp_ge_u32 s1, s33
	s_cselect_b32 s0, s2, s0
	s_cselect_b32 s1, s3, s1
	s_add_i32 s2, s0, 1
	s_cmp_ge_u32 s1, s33
	s_cselect_b32 s0, s2, s0
	v_readlane_b32 s1, v242, 30
	s_xor_b32 s0, s0, s1
	s_sub_i32 s0, s0, s1
	s_mul_i32 s1, s0, s33
	s_sub_i32 s1, s71, s1
	s_ashr_i32 s3, s1, 31
	s_lshr_b32 s3, s3, 30
	s_add_i32 s3, s1, s3
	s_mul_i32 s2, s0, 17
	s_ashr_i32 s4, s3, 2
	s_add_i32 s24, s4, s2
	s_and_b32 s2, s3, -4
	s_lshl_b32 s0, s0, 2
	s_sub_i32 s1, s1, s2
	s_add_i32 s22, s1, s0
	s_ashr_i32 s23, s22, 31
	s_lshl_b64 s[0:1], s[22:23], 19
	s_add_u32 s0, s39, s0
	s_addc_u32 s1, s40, s1
	s_ashr_i32 s25, s24, 31
	s_add_i32 s23, s12, 0x10000
	s_lshl_b64 s[2:3], s[24:25], 19
	s_add_i32 s25, s23, s11
	v_mov_b32_e32 v1, v211
	s_mov_b32 m0, s25
	s_add_i32 s42, s25, 0x2000
	global_load_lds_dwordx4 v1, s[0:1]
	v_mov_b32_e32 v1, v213
	s_add_u32 s4, s0, 0x40000
	s_mov_b32 m0, s42
	s_addc_u32 s5, s1, 0
	s_add_i32 s43, s12, 0x14000
	global_load_lds_dwordx4 v1, s[0:1]
	s_add_i32 s44, s43, s11
	v_mov_b32_e32 v1, v211
	s_mov_b32 m0, s44
	s_add_i32 s45, s44, 0x2000
	global_load_lds_dwordx4 v1, s[4:5]
	v_mov_b32_e32 v1, v213
	s_mov_b32 m0, s45
	s_add_u32 s2, s6, s2
	global_load_lds_dwordx4 v1, s[4:5]
	s_addc_u32 s3, s7, s3
	s_add_i32 s46, s12, s11
	v_mov_b32_e32 v1, v212
	s_mov_b32 m0, s46
	s_add_i32 s47, s46, 0x2000
	global_load_lds_dwordx4 v1, s[2:3]
	v_mov_b32_e32 v1, v214
	s_mov_b32 m0, s47
	s_add_u32 s4, s2, 0x40000
	global_load_lds_dwordx4 v1, s[2:3]
	s_addc_u32 s5, s3, 0
	s_add_i32 s48, s46, 0x4000
	v_mov_b32_e32 v1, v212
	s_mov_b32 m0, s48
	s_add_i32 s49, s46, 0x6000
	global_load_lds_dwordx4 v1, s[4:5]
	v_mov_b32_e32 v1, v214
	s_mov_b32 m0, s49
	s_cmp_eq_u32 s13, 1
	global_load_lds_dwordx4 v1, s[4:5]
	s_cselect_b64 s[4:5], -1, 0
	s_cmp_lg_u32 s13, 1
	s_cbranch_scc1 .LBB0_1469
	s_barrier

.LBB0_1515:
	s_mov_b32 s8, s84
	s_waitcnt vmcnt(0)
	s_waitcnt vmcnt(0) lgkmcnt(0)
	s_setprio 0
	s_barrier
	v_readlane_b32 s100, v242, 48
	s_nop 3
	s_cmp_lg_u32 s100, 1
	s_cbranch_scc1 .Lxb_skipinv_11
	buffer_inv sc1
